# PROJ epilogue full-128B-line stores via DPP half-row swap + B row permutation
# speedup vs baseline: 1.0033x; 1.0033x over previous
;     __device__ bool next(int i, Unit& u) const { const long L = (long)i * G + c; if (L >= nwg) return false; tile_of((int)L, nM, nN, u.pm, u.pn, wgm); u.z = 0; return true; }
; #define PG8_STAGE(bufoff, gbase, voff) do { _Pragma("unroll") for (int _i = 0; _i < 2; ++_i) \
;         __builtin_amdgcn_global_load_lds((const unsigned*)((const char*)(gbase) + (voff)[_i]), (PG8_LAS unsigned*)(lds + (bufoff) + ldsw + _i * 8192), 16, 0, 0); } while (0)
; #define PG8_WAIT_V(n) asm volatile("s_waitcnt vmcnt(" #n ")" ::: "memory")
; #define PG8_BAR __builtin_amdgcn_s_barrier()
; #define PG8_WAIT_V(n) asm volatile("s_waitcnt vmcnt(" #n ")" ::: "memory")
; template <class Epi, class Sched, bool ALIGN_EPI = true>
; __device__ __forceinline__ void gemm_phase(PG8_LAS unsigned char* lds, const Gemm g, const Sched& S, const Epi& E) {
;     ...
;     for (int i = 0; i < 2; ++i) { int R, C; stage_rc(tid * 16 + i * 8192, R, C); const int Rb = Epi::PERM ? ((R & ~31) + perm32(R & 31)) : R;
;         voffA[i] = (unsigned)(R * g.lda + C) * 2u; voffB[i] = (unsigned)(Rb * g.ldb + C) * 2u; }
;     const size_t kstep = (size_t)(BK * 2);
;     const size_t hA = (size_t)HALF * g.lda * 2, hB = (size_t)HALF * g.ldb * 2;
;     const size_t tA = 2 * hA, tB = 2 * hB;
;     const unsigned ldsw = (unsigned)wid * 1024u;
;     const int aoff = lds_byte(wr * 64 + fr, fq * 8), boff = lds_byte(wc * 32 + fr, fq * 8);
;     ...
;     Unit cur, nxt; int ui = 0;
;     if (!S.next(0, cur)) return;
;     f32x4 acc[2][2][4][2];
; #pragma unroll
;     for (int a = 0; a < 2; ++a)
; #pragma unroll
;         for (int b = 0; b < 2; ++b)
; #pragma unroll
;             for (int m = 0; m < 4; ++m)
; #pragma unroll
;                 for (int n = 0; n < 2; ++n) acc[a][b][m][n] = (f32x4){0.f, 0.f, 0.f, 0.f};
;     s16x8 At[4][2], B0[2][2], B1[2][2];
;     const char* cA = (const char*)(g.A + (long)cur.z * g.zA) + (size_t)cur.pm * tA; const char* cB = (const char*)(g.Bt + (long)cur.z * g.zB) + (size_t)cur.pn * tB;
;     PG8_STAGE(PG8_SB(0, 0), cB, voffB); PG8_STAGE(PG8_SB(0, 1), cB + hB, voffB); PG8_STAGE(PG8_SA(0, 0), cA, voffA); PG8_STAGE(PG8_SA(0, 1), cA + hA, voffA);
;     if (wr == 1) PG8_BAR;
;     PG8_WAIT_V(2); PG8_BAR;
;     PG8_STAGE(PG8_SB(1, 0), cB + kstep, voffB); PG8_STAGE(PG8_SA(1, 0), cA + kstep, voffA); PG8_STAGE(PG8_SB(1, 1), cB + hB + kstep, voffB);
;     PG8_WAIT_V(6); PG8_BAR;
.LBB0_971:
	s_or_b64 exec, exec, s[14:15]
	s_waitcnt vmcnt(0) lgkmcnt(0)
	v_readlane_b32 s0, v254, 6
	v_mov_b32_e32 v14, v243
	v_readlane_b32 s1, v254, 7
	s_barrier
	s_andn2_b64 vcc, exec, s[0:1]
	v_readfirstlane_b32 s14, v14
	s_cbranch_vccnz .LBB0_987
	v_lshlrev_b32_e32 v0, 4, v14
	v_add_u32_e32 v1, 0x2000, v0
	v_ashrrev_i32_e32 v2, 31, v1
	v_lshrrev_b32_e32 v2, 22, v2
	v_add_u32_e32 v2, v1, v2
	v_ashrrev_i32_e32 v8, 10, v2
	v_mul_i32_i24_e32 v2, 0x400, v8
	v_sub_u32_e32 v1, v1, v2
	v_lshrrev_b32_e32 v2, 4, v1
	v_bitop3_b32 v1, v2, v1, 32 bitop3:0x6c
	v_ashrrev_i32_e32 v2, 31, v1
	v_readlane_b32 s0, v255, 36
	v_lshrrev_b32_e32 v2, 26, v2
	v_readlane_b32 s1, v255, 37
	s_mov_b32 s4, s0
	v_add_u32_e32 v2, v1, v2
	v_lshlrev_b32_e32 v3, 3, v8
	s_mul_i32 s1, s4, 0x1200000
	v_readlane_b32 s4, v254, 4
	v_ashrrev_i32_e32 v9, 6, v2
	v_and_b32_e32 v3, -16, v3
	s_mul_hi_u32 s0, s0, 0x1200000
	v_readlane_b32 s5, v254, 5
	s_add_u32 s4, s4, s1
	v_add_u32_e32 v3, v9, v3
	s_addc_u32 s5, s5, s0
	v_and_b32_e32 v4, 3, v9
	s_mov_b32 s0, 0x1fffe0
	v_lshrrev_b32_e32 v5, 2, v3
	v_lshlrev_b32_e32 v6, 1, v3
	v_and_or_b32 v4, v3, s0, v4
	v_and_b32_e32 v5, 4, v5
	v_and_b32_e32 v6, 24, v6
	v_and_b32_e32 v2, 0xc0, v2
	v_or3_b32 v4, v4, v5, v6
	v_sub_u32_e32 v1, v1, v2
	v_mov_b32_e32 v6, 1
	v_lshlrev_b32_e32 v5, 5, v8
	v_ashrrev_i16_sdwa v1, v6, sext(v1) dst_sel:DWORD dst_unused:UNUSED_PAD src0_sel:DWORD src1_sel:BYTE_0
	v_and_b32_e32 v5, 32, v5
	v_bfe_i32 v10, v1, 0, 16
	v_add_lshl_u32 v1, v5, v10, 1
	v_lshl_add_u32 v130, v4, 11, v1
	v_and_b32_e32 v218, 0x30000, v130
	v_add_u32_e32 v130, v130, v218
	v_lshl_add_u32 v132, v3, 11, v1
	v_bfe_i32 v1, v14, 27, 1
	v_lshrrev_b32_e32 v1, 22, v1
	v_add_u32_e32 v1, v0, v1
	v_and_b32_e32 v1, 0xfffffc00, v1
	v_sub_u32_e32 v0, v0, v1
	v_lshrrev_b32_e32 v1, 4, v0
	v_ashrrev_i32_e32 v2, 31, v14
	v_bitop3_b32 v0, v1, v0, 32 bitop3:0x6c
	v_lshrrev_b32_e32 v2, 26, v2
	v_ashrrev_i32_e32 v1, 31, v0
	v_add_u32_e32 v2, v14, v2
	v_lshrrev_b32_e32 v1, 26, v1
	v_ashrrev_i32_e32 v12, 6, v2
	v_add_u32_e32 v1, v0, v1
	v_lshlrev_b32_e32 v2, 3, v12
	v_ashrrev_i32_e32 v11, 6, v1
	v_and_b32_e32 v2, -16, v2
	v_add_u32_e32 v2, v11, v2
	v_and_b32_e32 v3, 3, v11
	v_lshrrev_b32_e32 v4, 2, v2
	v_lshlrev_b32_e32 v5, 1, v2
	v_and_b32_e32 v1, 0xc0, v1
	s_ashr_i32 s15, s14, 6
	v_and_or_b32 v3, v2, s0, v3
	v_and_b32_e32 v4, 4, v4
	v_and_b32_e32 v5, 24, v5
	v_sub_u32_e32 v0, v0, v1
	s_ashr_i32 s19, s14, 8
	s_lshl_b32 s6, s15, 10
	v_or3_b32 v3, v3, v4, v5
	v_lshlrev_b32_e32 v4, 5, v12
	v_ashrrev_i16_sdwa v0, v6, sext(v0) dst_sel:DWORD dst_unused:UNUSED_PAD src0_sel:DWORD src1_sel:BYTE_0
	v_readlane_b32 s0, v254, 55
	v_and_b32_e32 v4, 32, v4
	v_bfe_i32 v13, v0, 0, 16
	v_readlane_b32 s1, v254, 56
	s_add_u32 s52, s4, s0
	v_add_lshl_u32 v0, v4, v13, 1
	s_addc_u32 s53, s5, s1
	s_add_i32 s10, s6, 0
	v_lshl_add_u32 v96, v3, 11, v0
	v_and_b32_e32 v218, 0x30000, v96
	v_add_u32_e32 v96, v96, v218
	s_add_i32 m0, s10, 0x10000
	v_lshl_add_u32 v134, v2, 11, v0
	global_load_lds_dwordx4 v96, s[52:53]
	s_add_i32 m0, s10, 0x12000
	s_add_u32 s0, s52, 0x10000
	global_load_lds_dwordx4 v130, s[52:53]
	s_addc_u32 s1, s53, 0
	s_add_i32 m0, s10, 0x14000
	v_mov_b32_e32 v131, v97
	global_load_lds_dwordx4 v96, s[0:1]
	s_add_i32 m0, s10, 0x16000
	v_mov_b32_e32 v135, v97
	global_load_lds_dwordx4 v130, s[0:1]
	v_readlane_b32 s0, v255, 9
	v_readlane_b32 s1, v255, 10
	s_add_u32 s50, s2, s0
	s_addc_u32 s51, s3, s1
	s_add_i32 s11, s10, 0x2000
	s_mov_b32 m0, s10
	s_add_u32 s0, s50, 0x40000
	global_load_lds_dwordx4 v134, s[50:51]
	s_mov_b32 m0, s11
	s_addc_u32 s1, s51, 0
	s_add_i32 s12, s10, 0x4000
	global_load_lds_dwordx4 v132, s[50:51]
	s_mov_b32 m0, s12
	s_add_i32 s13, s10, 0x6000
	global_load_lds_dwordx4 v134, s[0:1]
	s_mov_b32 m0, s13
	v_mov_b32_e32 v133, v97
	global_load_lds_dwordx4 v132, s[0:1]
	v_readlane_b32 s0, v252, 14
	v_readlane_b32 s1, v252, 15
	s_load_dword s18, s[0:1], 0x0
	s_cmp_eq_u32 s19, 1
	v_lshl_add_u64 v[6:7], s[52:53], 0, v[96:97]
	v_lshl_add_u64 v[4:5], s[52:53], 0, v[130:131]
	v_lshl_add_u64 v[0:1], s[50:51], 0, v[134:135]
	s_cselect_b64 s[0:1], -1, 0
	s_cmp_lg_u32 s19, 1
	v_lshl_add_u64 v[2:3], s[50:51], 0, v[132:133]
	s_cbranch_scc1 .LBB0_974
	s_barrier
.LBB0_974:
	v_lshrrev_b32_e32 v16, 1, v14
	v_and_b32_e32 v16, 24, v16
	v_and_b32_e32 v15, 15, v14
	v_lshlrev_b32_e32 v17, 1, v16
	v_lshlrev_b32_e32 v14, 2, v14
	s_lshl_b32 s15, s15, 5
	v_lshl_or_b32 v140, s19, 6, v15
	v_lshl_or_b32 v15, v15, 6, v17
	s_lshl_b32 s19, s19, 13
	v_and_b32_e32 v14, 32, v14
	s_and_b32 s28, s15, 0x60
	s_add_i32 m0, s10, 0x18000
	v_lshl_add_u64 v[6:7], v[6:7], 0, s[62:63]
	v_bitop3_b32 v17, v15, s19, v14 bitop3:0xde
	s_lshl_b32 s15, s28, 7
	s_waitcnt vmcnt(2)
	s_barrier
	global_load_lds_dwordx4 v[6:7], off
	v_lshl_add_u64 v[4:5], v[4:5], 0, s[62:63]
	s_add_i32 m0, s10, 0x1a000
	s_add_i32 s19, s10, 0x8000
	s_add_i32 s26, s10, 0xa000
	global_load_lds_dwordx4 v[4:5], off
	v_lshl_add_u64 v[0:1], v[0:1], 0, s[62:63]
	s_mov_b32 m0, s19
	s_add_u32 s20, s52, 0x10080
	global_load_lds_dwordx4 v[0:1], off
	v_lshl_add_u64 v[0:1], v[2:3], 0, s[62:63]
	s_mov_b32 m0, s26
	s_addc_u32 s21, s53, 0
	global_load_lds_dwordx4 v[0:1], off
	s_add_i32 m0, s10, 0x1c000
	v_lshl_add_u64 v[0:1], s[20:21], 0, v[96:97]
	global_load_lds_dwordx4 v[0:1], off
	v_lshl_add_u64 v[0:1], s[20:21], 0, v[130:131]
	s_add_i32 m0, s10, 0x1e000
	s_cmpk_lt_u32 s14, 0x100
	global_load_lds_dwordx4 v[0:1], off
	v_lshlrev_b32_e32 v0, 14, v12
	v_and_b32_e32 v0, 0xffff8000, v0
	v_lshl_add_u32 v0, v11, 11, v0
	v_and_b32_e32 v1, 1, v12
	v_lshl_or_b32 v0, v1, 6, v0
	v_lshl_add_u32 v136, v13, 1, v0
	v_lshlrev_b32_e32 v0, 14, v8
	v_and_b32_e32 v0, 0xffff8000, v0
	s_waitcnt vmcnt(6)
	v_lshl_add_u32 v0, v9, 11, v0
	v_and_b32_e32 v1, 1, v8
	v_lshl_or_b32 v0, v1, 6, v0
	v_readlane_b32 s20, v255, 7
	v_bitop3_b32 v141, v15, s15, v14 bitop3:0xde
	s_cselect_b64 s[14:15], -1, 0
	s_waitcnt lgkmcnt(0)
	s_ashr_i32 s27, s18, 31
	v_or_b32_e32 v142, s28, v16
	v_mov_b32_e32 v137, v97
	v_lshl_add_u32 v138, v10, 1, v0
	v_mov_b32_e32 v139, v97
	s_mov_b32 s28, 0
	v_add_u32_e32 v143, 0, v17
	v_readlane_b32 s34, v254, 54
	s_mov_b32 s35, s20
	s_barrier
	v_readlane_b32 s21, v255, 8
	s_branch .LBB0_977

; #define PG8_STAGE(bufoff, gbase, voff) do { _Pragma("unroll") for (int _i = 0; _i < 2; ++_i) \
;         __builtin_amdgcn_global_load_lds((const unsigned*)((const char*)(gbase) + (voff)[_i]), (PG8_LAS unsigned*)(lds + (bufoff) + ldsw + _i * 8192), 16, 0, 0); } while (0)
; #define PG8_LDA(dst, b, h) do { _Pragma("unroll") for (int m = 0; m < 4; ++m) _Pragma("unroll") for (int k = 0; k < 2; ++k) dst[m][k] = *(const PG8_LAS s16x8*)(lds + PG8_SA(b, h) + aoff + m * 2048 + k * 1024); } while (0)
; #define PG8_LDB(dst, b, h) do { _Pragma("unroll") for (int n = 0; n < 2; ++n) _Pragma("unroll") for (int k = 0; k < 2; ++k) dst[n][k] = *(const PG8_LAS s16x8*)(lds + PG8_SB(b, h) + boff + n * 2048 + k * 1024); } while (0)
; #define PG8_WAIT_V(n) asm volatile("s_waitcnt vmcnt(" #n ")" ::: "memory")
; #define PG8_WAIT_L(n) asm volatile("s_waitcnt lgkmcnt(" #n ")" ::: "memory")
; #define PG8_BAR __builtin_amdgcn_s_barrier()
; #define PG8_SCHED __builtin_amdgcn_sched_barrier(0)
; #define PG8_STAGE(bufoff, gbase, voff) do { _Pragma("unroll") for (int _i = 0; _i < 2; ++_i) \
;         __builtin_amdgcn_global_load_lds((const unsigned*)((const char*)(gbase) + (voff)[_i]), (PG8_LAS unsigned*)(lds + (bufoff) + ldsw + _i * 8192), 16, 0, 0); } while (0)
; #define PG8_WAIT_V(n) asm volatile("s_waitcnt vmcnt(" #n ")" ::: "memory")
; template <class Epi, class Sched, bool ALIGN_EPI = true>
; __device__ __forceinline__ void gemm_phase(PG8_LAS unsigned char* lds, const Gemm g, const Sched& S, const Epi& E) {
;     ...
;         for (int t = 0; t < nt; t += 2) {
;             const bool last = (t == nt - 2);
;             const char* a1 = cA + (size_t)(t + 1) * kstep;
;             const char* a2 = last ? nA : cA + (size_t)(t + 2) * kstep; const char* b2 = last ? nB : cB + (size_t)(t + 2) * kstep;
;             const char* a3 = a2 + kstep; const char* b3 = b2 + kstep;
;             PG8_LDB(B0, 0, 0); PG8_LDB(B1, 0, 1); PG8_SCHED; PG8_LDA(At, 0, 0); PG8_STAGE(PG8_SA(1, 1), a1 + hA, voffA);
;             PG8_WAIT_V(8); PG8_WAIT_L(0); PG8_BAR; PG8_MMA(0, 0, At, B0); PG8_MMA(0, 1, At, B1); PG8_BAR; PG8_SCHED;
;             PG8_LDA(At, 0, 1); PG8_STAGE(PG8_SB(0, 0), b2, voffB); PG8_STAGE(PG8_SB(0, 1), b2 + hB, voffB); PG8_STAGE(PG8_SA(0, 0), a2, voffA);
;             PG8_WAIT_V(8); PG8_WAIT_L(0); PG8_BAR; PG8_MMA(1, 0, At, B0); PG8_MMA(1, 1, At, B1); PG8_BAR; PG8_SCHED;
.LBB0_980:
	s_add_u32 s52, s50, 0xfffc0080
	s_addc_u32 s53, s51, -1
	s_add_i32 s57, 0, 0x10000
	s_cmp_eq_u32 s56, 12
	s_cselect_b32 s55, s36, s53
	s_cselect_b32 s54, s37, s52
	s_cselect_b32 s53, s21, s45
	s_cselect_b32 s52, s41, s44
	s_add_i32 s60, 0, 0x14000
	v_add_u32_e32 v156, s57, v141
	v_add_u32_e32 v172, s60, v141
	ds_read_b128 v[144:147], v156
	ds_read_b128 v[148:151], v156 offset:1024
	ds_read_b128 v[152:155], v156 offset:2048
	ds_read_b128 v[156:159], v156 offset:3072
	ds_read_b128 v[160:163], v172
	ds_read_b128 v[164:167], v172 offset:1024
	ds_read_b128 v[168:171], v172 offset:2048
	ds_read_b128 v[172:175], v172 offset:3072
	v_lshl_add_u64 v[208:209], s[50:51], 0, v[136:137]
	s_add_i32 m0, s10, 0xc000
	ds_read_b128 v[176:179], v143
	ds_read_b128 v[180:183], v143 offset:1024
	ds_read_b128 v[184:187], v143 offset:2048
	ds_read_b128 v[188:191], v143 offset:3072
	ds_read_b128 v[192:195], v143 offset:4096
	ds_read_b128 v[196:199], v143 offset:5120
	ds_read_b128 v[200:203], v143 offset:6144
	ds_read_b128 v[204:207], v143 offset:7168
	global_load_lds_dwordx4 v[208:209], off
	v_lshl_add_u64 v[208:209], s[50:51], 0, v[138:139]
	s_add_i32 m0, s10, 0xe000
	s_nop 0
	global_load_lds_dwordx4 v[208:209], off
	s_waitcnt vmcnt(8)
	s_waitcnt lgkmcnt(0)
	s_barrier
	s_setprio 1
	s_waitcnt lgkmcnt(0)
	v_mfma_f32_16x16x32_f16 v[126:129], v[144:147], v[176:179], v[126:129]
	v_mfma_f32_16x16x32_f16 v[122:125], v[152:155], v[176:179], v[122:125]
	v_mfma_f32_16x16x32_f16 v[118:121], v[144:147], v[184:187], v[118:121]
	v_mfma_f32_16x16x32_f16 v[114:117], v[152:155], v[184:187], v[114:117]
	v_mfma_f32_16x16x32_f16 v[102:105], v[144:147], v[192:195], v[102:105]
	v_mfma_f32_16x16x32_f16 v[98:101], v[152:155], v[192:195], v[98:101]
	v_mfma_f32_16x16x32_f16 v[84:87], v[144:147], v[200:203], v[84:87]
	v_mfma_f32_16x16x32_f16 v[80:83], v[152:155], v[200:203], v[80:83]
	v_mfma_f32_16x16x32_f16 v[126:129], v[148:151], v[180:183], v[126:129]
	v_mfma_f32_16x16x32_f16 v[122:125], v[156:159], v[180:183], v[122:125]
	v_mfma_f32_16x16x32_f16 v[118:121], v[148:151], v[188:191], v[118:121]
	v_mfma_f32_16x16x32_f16 v[114:117], v[156:159], v[188:191], v[114:117]
	v_mfma_f32_16x16x32_f16 v[102:105], v[148:151], v[196:199], v[102:105]
	v_mfma_f32_16x16x32_f16 v[98:101], v[156:159], v[196:199], v[98:101]
	v_mfma_f32_16x16x32_f16 v[84:87], v[148:151], v[204:207], v[84:87]
	v_mfma_f32_16x16x32_f16 v[80:83], v[156:159], v[204:207], v[80:83]
	s_setprio 0
	s_setprio 1
	v_mfma_f32_16x16x32_f16 v[110:113], v[160:163], v[176:179], v[110:113]
	v_mfma_f32_16x16x32_f16 v[106:109], v[168:171], v[176:179], v[106:109]
	v_mfma_f32_16x16x32_f16 v[92:95], v[160:163], v[184:187], v[92:95]
	v_mfma_f32_16x16x32_f16 v[88:91], v[168:171], v[184:187], v[88:91]
	v_mfma_f32_16x16x32_f16 v[76:79], v[160:163], v[192:195], v[76:79]
	v_mfma_f32_16x16x32_f16 v[72:75], v[168:171], v[192:195], v[72:75]
	v_mfma_f32_16x16x32_f16 v[68:71], v[160:163], v[200:203], v[68:71]
	v_mfma_f32_16x16x32_f16 v[64:67], v[168:171], v[200:203], v[64:67]
	v_mfma_f32_16x16x32_f16 v[110:113], v[164:167], v[180:183], v[110:113]
	v_mfma_f32_16x16x32_f16 v[106:109], v[172:175], v[180:183], v[106:109]
	v_mfma_f32_16x16x32_f16 v[92:95], v[164:167], v[188:191], v[92:95]
	v_mfma_f32_16x16x32_f16 v[88:91], v[172:175], v[188:191], v[88:91]
	v_mfma_f32_16x16x32_f16 v[76:79], v[164:167], v[196:199], v[76:79]
	v_mfma_f32_16x16x32_f16 v[72:75], v[172:175], v[196:199], v[72:75]
	v_mfma_f32_16x16x32_f16 v[68:71], v[164:167], v[204:207], v[68:71]
	v_mfma_f32_16x16x32_f16 v[64:67], v[172:175], v[204:207], v[64:67]
	s_setprio 0
	s_barrier
	s_add_i32 s57, s57, s6
	v_lshl_add_u64 v[208:209], s[52:53], 0, v[96:97]
	s_mov_b32 m0, s57
	ds_read_b128 v[176:179], v143 offset:16384
	ds_read_b128 v[180:183], v143 offset:17408
	ds_read_b128 v[184:187], v143 offset:18432
	ds_read_b128 v[188:191], v143 offset:19456
	ds_read_b128 v[192:195], v143 offset:20480
	ds_read_b128 v[196:199], v143 offset:21504
	ds_read_b128 v[200:203], v143 offset:22528
	ds_read_b128 v[204:207], v143 offset:23552
	global_load_lds_dwordx4 v[208:209], off
	s_add_i32 m0, s57, 0x2000
	s_add_u32 s58, s52, 0x10000
	v_lshl_add_u64 v[210:211], s[52:53], 0, v[130:131]
	s_addc_u32 s59, s53, 0
	s_add_i32 s57, s60, s6
	global_load_lds_dwordx4 v[210:211], off
	v_lshl_add_u64 v[212:213], s[58:59], 0, v[96:97]
	s_mov_b32 m0, s57
	v_lshl_add_u64 v[214:215], s[54:55], 0, v[132:133]
	global_load_lds_dwordx4 v[212:213], off
	v_lshl_add_u64 v[212:213], s[58:59], 0, v[130:131]
	s_add_i32 m0, s57, 0x2000
	s_nop 0
	global_load_lds_dwordx4 v[212:213], off
	v_lshl_add_u64 v[212:213], s[54:55], 0, v[134:135]
	s_mov_b32 m0, s10
	s_nop 0
	global_load_lds_dwordx4 v[212:213], off
	s_mov_b32 m0, s11
	s_nop 0
	global_load_lds_dwordx4 v[214:215], off
	s_waitcnt vmcnt(8)
	s_waitcnt lgkmcnt(0)
	s_barrier
; #define PG8_STAGE(bufoff, gbase, voff) do { _Pragma("unroll") for (int _i = 0; _i < 2; ++_i) \
;         __builtin_amdgcn_global_load_lds((const unsigned*)((const char*)(gbase) + (voff)[_i]), (PG8_LAS unsigned*)(lds + (bufoff) + ldsw + _i * 8192), 16, 0, 0); } while (0)
; #define PG8_LDA(dst, b, h) do { _Pragma("unroll") for (int m = 0; m < 4; ++m) _Pragma("unroll") for (int k = 0; k < 2; ++k) dst[m][k] = *(const PG8_LAS s16x8*)(lds + PG8_SA(b, h) + aoff + m * 2048 + k * 1024); } while (0)
; #define PG8_LDB(dst, b, h) do { _Pragma("unroll") for (int n = 0; n < 2; ++n) _Pragma("unroll") for (int k = 0; k < 2; ++k) dst[n][k] = *(const PG8_LAS s16x8*)(lds + PG8_SB(b, h) + boff + n * 2048 + k * 1024); } while (0)
; #define PG8_WAIT_V(n) asm volatile("s_waitcnt vmcnt(" #n ")" ::: "memory")
; #define PG8_WAIT_L(n) asm volatile("s_waitcnt lgkmcnt(" #n ")" ::: "memory")
; #define PG8_BAR __builtin_amdgcn_s_barrier()
; #define PG8_SCHED __builtin_amdgcn_sched_barrier(0)
; #define PG8_STAGE(bufoff, gbase, voff) do { _Pragma("unroll") for (int _i = 0; _i < 2; ++_i) \
;         __builtin_amdgcn_global_load_lds((const unsigned*)((const char*)(gbase) + (voff)[_i]), (PG8_LAS unsigned*)(lds + (bufoff) + ldsw + _i * 8192), 16, 0, 0); } while (0)
; #define PG8_LDA(dst, b, h) do { _Pragma("unroll") for (int m = 0; m < 4; ++m) _Pragma("unroll") for (int k = 0; k < 2; ++k) dst[m][k] = *(const PG8_LAS s16x8*)(lds + PG8_SA(b, h) + aoff + m * 2048 + k * 1024); } while (0)
; #define PG8_LDB(dst, b, h) do { _Pragma("unroll") for (int n = 0; n < 2; ++n) _Pragma("unroll") for (int k = 0; k < 2; ++k) dst[n][k] = *(const PG8_LAS s16x8*)(lds + PG8_SB(b, h) + boff + n * 2048 + k * 1024); } while (0)
; #define PG8_WAIT_V(n) asm volatile("s_waitcnt vmcnt(" #n ")" ::: "memory")
; #define PG8_WAIT_L(n) asm volatile("s_waitcnt lgkmcnt(" #n ")" ::: "memory")
; template <class Epi, class Sched, bool ALIGN_EPI = true>
; __device__ __forceinline__ void gemm_phase(PG8_LAS unsigned char* lds, const Gemm g, const Sched& S, const Epi& E) {
;     ...
;             PG8_WAIT_V(8); PG8_WAIT_L(0); PG8_BAR; PG8_MMA(1, 0, At, B0); PG8_MMA(1, 1, At, B1); PG8_BAR; PG8_SCHED;
;             PG8_LDB(B0, 1, 0); PG8_LDB(B1, 1, 1); PG8_SCHED; PG8_LDA(At, 1, 0); PG8_STAGE(PG8_SA(0, 1), a2 + hA, voffA);
;             PG8_WAIT_V(8); PG8_WAIT_L(0); PG8_BAR; PG8_MMA(0, 0, At, B0); PG8_MMA(0, 1, At, B1); PG8_BAR; PG8_SCHED;
	s_setprio 1
	s_waitcnt lgkmcnt(0)
	v_mfma_f32_16x16x32_f16 v[60:63], v[144:147], v[176:179], v[60:63]
	v_mfma_f32_16x16x32_f16 v[56:59], v[152:155], v[176:179], v[56:59]
	v_mfma_f32_16x16x32_f16 v[52:55], v[144:147], v[184:187], v[52:55]
	v_mfma_f32_16x16x32_f16 v[48:51], v[152:155], v[184:187], v[48:51]
	v_mfma_f32_16x16x32_f16 v[36:39], v[144:147], v[192:195], v[36:39]
	v_mfma_f32_16x16x32_f16 v[32:35], v[152:155], v[192:195], v[32:35]
	v_mfma_f32_16x16x32_f16 v[20:23], v[144:147], v[200:203], v[20:23]
	v_mfma_f32_16x16x32_f16 v[16:19], v[152:155], v[200:203], v[16:19]
	v_mfma_f32_16x16x32_f16 v[60:63], v[148:151], v[180:183], v[60:63]
	v_mfma_f32_16x16x32_f16 v[56:59], v[156:159], v[180:183], v[56:59]
	v_mfma_f32_16x16x32_f16 v[52:55], v[148:151], v[188:191], v[52:55]
	v_mfma_f32_16x16x32_f16 v[48:51], v[156:159], v[188:191], v[48:51]
	v_mfma_f32_16x16x32_f16 v[36:39], v[148:151], v[196:199], v[36:39]
	v_mfma_f32_16x16x32_f16 v[32:35], v[156:159], v[196:199], v[32:35]
	v_mfma_f32_16x16x32_f16 v[20:23], v[148:151], v[204:207], v[20:23]
	v_mfma_f32_16x16x32_f16 v[16:19], v[156:159], v[204:207], v[16:19]
	s_setprio 0
	s_setprio 1
	v_mfma_f32_16x16x32_f16 v[44:47], v[160:163], v[176:179], v[44:47]
	v_mfma_f32_16x16x32_f16 v[40:43], v[168:171], v[176:179], v[40:43]
	v_mfma_f32_16x16x32_f16 v[28:31], v[160:163], v[184:187], v[28:31]
	v_mfma_f32_16x16x32_f16 v[24:27], v[168:171], v[184:187], v[24:27]
	v_mfma_f32_16x16x32_f16 v[12:15], v[160:163], v[192:195], v[12:15]
	v_mfma_f32_16x16x32_f16 v[8:11], v[168:171], v[192:195], v[8:11]
	v_mfma_f32_16x16x32_f16 v[4:7], v[160:163], v[200:203], v[4:7]
	v_mfma_f32_16x16x32_f16 v[0:3], v[168:171], v[200:203], v[0:3]
	v_mfma_f32_16x16x32_f16 v[44:47], v[164:167], v[180:183], v[44:47]
	v_mfma_f32_16x16x32_f16 v[40:43], v[172:175], v[180:183], v[40:43]
	v_mfma_f32_16x16x32_f16 v[28:31], v[164:167], v[188:191], v[28:31]
	v_mfma_f32_16x16x32_f16 v[24:27], v[172:175], v[188:191], v[24:27]
	v_mfma_f32_16x16x32_f16 v[12:15], v[164:167], v[196:199], v[12:15]
	v_mfma_f32_16x16x32_f16 v[8:11], v[172:175], v[196:199], v[8:11]
	v_mfma_f32_16x16x32_f16 v[4:7], v[164:167], v[204:207], v[4:7]
	v_mfma_f32_16x16x32_f16 v[0:3], v[172:175], v[204:207], v[0:3]
	s_setprio 0
	s_barrier
	s_add_i32 s57, 0, 0x18000
	s_add_i32 s58, 0, 0x1c000
	v_add_u32_e32 v156, s57, v141
	v_add_u32_e32 v172, s58, v141
	ds_read_b128 v[144:147], v156
	ds_read_b128 v[148:151], v156 offset:1024
	ds_read_b128 v[152:155], v156 offset:2048
	ds_read_b128 v[156:159], v156 offset:3072
	ds_read_b128 v[160:163], v172
	ds_read_b128 v[164:167], v172 offset:1024
	ds_read_b128 v[168:171], v172 offset:2048
	ds_read_b128 v[172:175], v172 offset:3072
	s_add_u32 s54, s54, 0x40000
	s_addc_u32 s55, s55, 0
	s_mov_b32 m0, s12
	v_lshl_add_u64 v[216:217], s[54:55], 0, v[134:135]
	ds_read_b128 v[176:179], v143 offset:32768
	ds_read_b128 v[180:183], v143 offset:33792
	ds_read_b128 v[184:187], v143 offset:34816
	ds_read_b128 v[188:191], v143 offset:35840
	ds_read_b128 v[192:195], v143 offset:36864
	ds_read_b128 v[196:199], v143 offset:37888
	ds_read_b128 v[200:203], v143 offset:38912
	ds_read_b128 v[204:207], v143 offset:39936
	global_load_lds_dwordx4 v[216:217], off
	v_lshl_add_u64 v[216:217], s[54:55], 0, v[132:133]
	s_mov_b32 m0, s13
	s_nop 0
	global_load_lds_dwordx4 v[216:217], off
	s_waitcnt vmcnt(8)
	s_waitcnt lgkmcnt(0)
	s_barrier
	s_setprio 1
	s_waitcnt lgkmcnt(0)
	v_mfma_f32_16x16x32_f16 v[126:129], v[144:147], v[176:179], v[126:129]
	v_mfma_f32_16x16x32_f16 v[122:125], v[152:155], v[176:179], v[122:125]
	v_mfma_f32_16x16x32_f16 v[118:121], v[144:147], v[184:187], v[118:121]
	v_mfma_f32_16x16x32_f16 v[114:117], v[152:155], v[184:187], v[114:117]
	v_mfma_f32_16x16x32_f16 v[102:105], v[144:147], v[192:195], v[102:105]
	v_mfma_f32_16x16x32_f16 v[98:101], v[152:155], v[192:195], v[98:101]
	v_mfma_f32_16x16x32_f16 v[84:87], v[144:147], v[200:203], v[84:87]
	v_mfma_f32_16x16x32_f16 v[80:83], v[152:155], v[200:203], v[80:83]
	v_mfma_f32_16x16x32_f16 v[126:129], v[148:151], v[180:183], v[126:129]
	v_mfma_f32_16x16x32_f16 v[122:125], v[156:159], v[180:183], v[122:125]
	v_mfma_f32_16x16x32_f16 v[118:121], v[148:151], v[188:191], v[118:121]
	v_mfma_f32_16x16x32_f16 v[114:117], v[156:159], v[188:191], v[114:117]
	v_mfma_f32_16x16x32_f16 v[102:105], v[148:151], v[196:199], v[102:105]
	v_mfma_f32_16x16x32_f16 v[98:101], v[156:159], v[196:199], v[98:101]
	v_mfma_f32_16x16x32_f16 v[84:87], v[148:151], v[204:207], v[84:87]
	v_mfma_f32_16x16x32_f16 v[80:83], v[156:159], v[204:207], v[80:83]
	s_setprio 0
	s_setprio 1
	v_mfma_f32_16x16x32_f16 v[110:113], v[160:163], v[176:179], v[110:113]
	v_mfma_f32_16x16x32_f16 v[106:109], v[168:171], v[176:179], v[106:109]
	v_mfma_f32_16x16x32_f16 v[92:95], v[160:163], v[184:187], v[92:95]
	v_mfma_f32_16x16x32_f16 v[88:91], v[168:171], v[184:187], v[88:91]
	v_mfma_f32_16x16x32_f16 v[76:79], v[160:163], v[192:195], v[76:79]
	v_mfma_f32_16x16x32_f16 v[72:75], v[168:171], v[192:195], v[72:75]
	v_mfma_f32_16x16x32_f16 v[68:71], v[160:163], v[200:203], v[68:71]
	v_mfma_f32_16x16x32_f16 v[64:67], v[168:171], v[200:203], v[64:67]
	v_mfma_f32_16x16x32_f16 v[110:113], v[164:167], v[180:183], v[110:113]
	v_mfma_f32_16x16x32_f16 v[106:109], v[172:175], v[180:183], v[106:109]
	v_mfma_f32_16x16x32_f16 v[92:95], v[164:167], v[188:191], v[92:95]
	v_mfma_f32_16x16x32_f16 v[88:91], v[172:175], v[188:191], v[88:91]
	v_mfma_f32_16x16x32_f16 v[76:79], v[164:167], v[196:199], v[76:79]
	v_mfma_f32_16x16x32_f16 v[72:75], v[172:175], v[196:199], v[72:75]
	v_mfma_f32_16x16x32_f16 v[68:71], v[164:167], v[204:207], v[68:71]
	v_mfma_f32_16x16x32_f16 v[64:67], v[172:175], v[204:207], v[64:67]
	s_setprio 0
	s_barrier
; #define PG8_STAGE(bufoff, gbase, voff) do { _Pragma("unroll") for (int _i = 0; _i < 2; ++_i) \
;         __builtin_amdgcn_global_load_lds((const unsigned*)((const char*)(gbase) + (voff)[_i]), (PG8_LAS unsigned*)(lds + (bufoff) + ldsw + _i * 8192), 16, 0, 0); } while (0)
; #define PG8_LDA(dst, b, h) do { _Pragma("unroll") for (int m = 0; m < 4; ++m) _Pragma("unroll") for (int k = 0; k < 2; ++k) dst[m][k] = *(const PG8_LAS s16x8*)(lds + PG8_SA(b, h) + aoff + m * 2048 + k * 1024); } while (0)
; #define PG8_WAIT_V(n) asm volatile("s_waitcnt vmcnt(" #n ")" ::: "memory")
; #define PG8_WAIT_L(n) asm volatile("s_waitcnt lgkmcnt(" #n ")" ::: "memory")
; #define PG8_BAR __builtin_amdgcn_s_barrier()
; #define PG8_SCHED __builtin_amdgcn_sched_barrier(0)
; #define PG8_STAGE(bufoff, gbase, voff) do { _Pragma("unroll") for (int _i = 0; _i < 2; ++_i) \
;         __builtin_amdgcn_global_load_lds((const unsigned*)((const char*)(gbase) + (voff)[_i]), (PG8_LAS unsigned*)(lds + (bufoff) + ldsw + _i * 8192), 16, 0, 0); } while (0)
; #define PG8_LDA(dst, b, h) do { _Pragma("unroll") for (int m = 0; m < 4; ++m) _Pragma("unroll") for (int k = 0; k < 2; ++k) dst[m][k] = *(const PG8_LAS s16x8*)(lds + PG8_SA(b, h) + aoff + m * 2048 + k * 1024); } while (0)
; #define PG8_WAIT_V(n) asm volatile("s_waitcnt vmcnt(" #n ")" ::: "memory")
; #define PG8_BAR __builtin_amdgcn_s_barrier()
;     __device__ __forceinline__ void operator()(const f32x4 (&acc)[2][2][4][2], const Unit& u, int wr, int wc, int fr, int fq) const {
;         const int row0 = u.pm * BM + wr * 64 + fr, col0 = u.pn * BM + wc * 32 + 8 * fq;
; #pragma unroll
;         for (int ai = 0; ai < 2; ++ai)
; #pragma unroll
;             for (int m = 0; m < 4; ++m) { h16* rowp = C + (size_t)(row0 + ai * HALF + m * 16) * ldc + col0;
; template <class Epi, class Sched, bool ALIGN_EPI = true>
; __device__ __forceinline__ void gemm_phase(PG8_LAS unsigned char* lds, const Gemm g, const Sched& S, const Epi& E) {
;     ...
;             PG8_LDA(At, 1, 1); PG8_STAGE(PG8_SB(1, 0), b3, voffB); PG8_STAGE(PG8_SB(1, 1), b3 + hB, voffB); PG8_STAGE(PG8_SA(1, 0), a3, voffA);
;             PG8_WAIT_V(8); PG8_WAIT_L(0); PG8_BAR; PG8_MMA(1, 0, At, B0); PG8_MMA(1, 1, At, B1); PG8_BAR; PG8_SCHED;
;         }
;         if constexpr (ALIGN_EPI) { if (wr == 0) PG8_BAR; }
;         if constexpr (!Epi::AFTER_DRAIN) E(acc, cur, wr, wc, fr, fq);
	s_add_i32 s54, s57, s6
	v_lshl_add_u64 v[208:209], v[208:209], 0, s[62:63]
	s_mov_b32 m0, s54
	ds_read_b128 v[176:179], v143 offset:49152
	ds_read_b128 v[180:183], v143 offset:50176
	ds_read_b128 v[184:187], v143 offset:51200
	ds_read_b128 v[188:191], v143 offset:52224
	ds_read_b128 v[192:195], v143 offset:53248
	ds_read_b128 v[196:199], v143 offset:54272
	ds_read_b128 v[200:203], v143 offset:55296
	ds_read_b128 v[204:207], v143 offset:56320
	global_load_lds_dwordx4 v[208:209], off
	s_add_i32 m0, s54, 0x2000
	s_add_u32 s52, s52, 0x10080
	v_lshl_add_u64 v[208:209], v[210:211], 0, s[62:63]
	s_addc_u32 s53, s53, 0
	s_add_i32 s54, s58, s6
	global_load_lds_dwordx4 v[208:209], off
	v_lshl_add_u64 v[208:209], s[52:53], 0, v[96:97]
	s_mov_b32 m0, s54
	s_nop 0
	global_load_lds_dwordx4 v[208:209], off
	v_lshl_add_u64 v[208:209], s[52:53], 0, v[130:131]
	s_add_i32 m0, s54, 0x2000
	s_nop 0
	global_load_lds_dwordx4 v[208:209], off
	v_lshl_add_u64 v[208:209], v[212:213], 0, s[62:63]
	s_mov_b32 m0, s19
	s_nop 0
	global_load_lds_dwordx4 v[208:209], off
	v_lshl_add_u64 v[208:209], v[214:215], 0, s[62:63]
	s_mov_b32 m0, s26
	s_nop 0
	global_load_lds_dwordx4 v[208:209], off
	s_waitcnt vmcnt(8)
	s_waitcnt lgkmcnt(0)
	s_barrier
	s_setprio 1
	s_waitcnt lgkmcnt(0)
	v_mfma_f32_16x16x32_f16 v[60:63], v[144:147], v[176:179], v[60:63]
	v_mfma_f32_16x16x32_f16 v[56:59], v[152:155], v[176:179], v[56:59]
	v_mfma_f32_16x16x32_f16 v[52:55], v[144:147], v[184:187], v[52:55]
	v_mfma_f32_16x16x32_f16 v[48:51], v[152:155], v[184:187], v[48:51]
	v_mfma_f32_16x16x32_f16 v[36:39], v[144:147], v[192:195], v[36:39]
	v_mfma_f32_16x16x32_f16 v[32:35], v[152:155], v[192:195], v[32:35]
	v_mfma_f32_16x16x32_f16 v[20:23], v[144:147], v[200:203], v[20:23]
	v_mfma_f32_16x16x32_f16 v[16:19], v[152:155], v[200:203], v[16:19]
	v_mfma_f32_16x16x32_f16 v[60:63], v[148:151], v[180:183], v[60:63]
	v_mfma_f32_16x16x32_f16 v[56:59], v[156:159], v[180:183], v[56:59]
	v_mfma_f32_16x16x32_f16 v[52:55], v[148:151], v[188:191], v[52:55]
	v_mfma_f32_16x16x32_f16 v[48:51], v[156:159], v[188:191], v[48:51]
	v_mfma_f32_16x16x32_f16 v[36:39], v[148:151], v[196:199], v[36:39]
	v_mfma_f32_16x16x32_f16 v[32:35], v[156:159], v[196:199], v[32:35]
	v_mfma_f32_16x16x32_f16 v[20:23], v[148:151], v[204:207], v[20:23]
	v_mfma_f32_16x16x32_f16 v[16:19], v[156:159], v[204:207], v[16:19]
	s_setprio 0
	s_setprio 1
	v_mfma_f32_16x16x32_f16 v[44:47], v[160:163], v[176:179], v[44:47]
	v_mfma_f32_16x16x32_f16 v[40:43], v[168:171], v[176:179], v[40:43]
	v_mfma_f32_16x16x32_f16 v[28:31], v[160:163], v[184:187], v[28:31]
	v_mfma_f32_16x16x32_f16 v[24:27], v[168:171], v[184:187], v[24:27]
	v_mfma_f32_16x16x32_f16 v[12:15], v[160:163], v[192:195], v[12:15]
	v_mfma_f32_16x16x32_f16 v[8:11], v[168:171], v[192:195], v[8:11]
	v_mfma_f32_16x16x32_f16 v[4:7], v[160:163], v[200:203], v[4:7]
	v_mfma_f32_16x16x32_f16 v[0:3], v[168:171], v[200:203], v[0:3]
	v_mfma_f32_16x16x32_f16 v[44:47], v[164:167], v[180:183], v[44:47]
	v_mfma_f32_16x16x32_f16 v[40:43], v[172:175], v[180:183], v[40:43]
	v_mfma_f32_16x16x32_f16 v[28:31], v[164:167], v[188:191], v[28:31]
	v_mfma_f32_16x16x32_f16 v[24:27], v[172:175], v[188:191], v[24:27]
	v_mfma_f32_16x16x32_f16 v[12:15], v[164:167], v[196:199], v[12:15]
	v_mfma_f32_16x16x32_f16 v[8:11], v[172:175], v[196:199], v[8:11]
	v_mfma_f32_16x16x32_f16 v[4:7], v[164:167], v[204:207], v[4:7]
	v_mfma_f32_16x16x32_f16 v[0:3], v[172:175], v[204:207], v[0:3]
	s_setprio 0
	s_barrier
	s_add_i32 s56, s56, 2
	s_add_u32 s50, s50, 0x100
	s_addc_u32 s51, s51, 0
	s_add_u32 s44, s44, 0x100
	s_addc_u32 s45, s45, 0
	s_cmp_gt_u32 s56, 13
	s_cbranch_scc0 .LBB0_980
	s_and_b64 vcc, exec, s[14:15]
	s_cbranch_vccz .LBB0_983
	s_barrier
.LBB0_983:
	v_and_b32_e32 v224, -9, v140
	v_and_b32_e32 v225, 8, v140
	v_and_b32_e32 v226, 0x60, v142
	v_lshlrev_b32_e32 v225, 2, v225
	v_add3_u32 v226, v142, v226, v225
	v_lshl_add_u32 v150, s35, 8, v224
	v_lshl_or_b32 v144, s34, 8, v226
	v_ashrrev_i32_e32 v145, 31, v144
	v_mov_b64_e32 v[146:147], s[16:17]
	v_lshlrev_b64 v[144:145], 1, v[144:145]
	s_mov_b64 s[52:53], 0x1c000
	v_mad_i64_i32 v[152:153], s[34:35], v150, s91, v[146:147]
	v_lshl_add_u64 v[152:153], v[152:153], 0, v[144:145]
	v_add_u32_e32 v151, 0x10, v150
	v_mad_i64_i32 v[154:155], s[34:35], v151, s91, v[146:147]
	v_lshl_add_u64 v[154:155], v[154:155], 0, v[144:145]
	v_add_u32_e32 v151, 0x20, v150
	v_mad_i64_i32 v[156:157], s[34:35], v151, s91, v[146:147]
	v_lshl_add_u64 v[156:157], v[156:157], 0, v[144:145]
	v_add_u32_e32 v151, 0x30, v150
	v_mad_i64_i32 v[158:159], s[34:35], v151, s91, v[146:147]
	v_lshl_add_u64 v[158:159], v[158:159], 0, v[144:145]
	v_add_u32_e32 v151, 0x80, v150
	v_mad_i64_i32 v[160:161], s[34:35], v151, s91, v[146:147]
	v_lshl_add_u64 v[160:161], v[160:161], 0, v[144:145]
	v_add_u32_e32 v151, 0x90, v150
	v_mad_i64_i32 v[162:163], s[34:35], v151, s91, v[146:147]
	v_lshl_add_u64 v[162:163], v[162:163], 0, v[144:145]
	v_add_u32_e32 v151, 0xa0, v150
	v_mad_i64_i32 v[164:165], s[34:35], v151, s91, v[146:147]
	v_lshl_add_u64 v[164:165], v[164:165], 0, v[144:145]
	v_add_u32_e32 v151, 0xb0, v150
	v_mad_i64_i32 v[166:167], s[34:35], v151, s91, v[146:147]
	v_lshl_add_u64 v[166:167], v[166:167], 0, v[144:145]
	v_cvt_pk_f16_f32 v126, v126, v127
	v_cvt_pk_f16_f32 v127, v128, v129
	v_cvt_pk_f16_f32 v128, v122, v123
	v_cvt_pk_f16_f32 v129, v124, v125
	v_cvt_pk_f16_f32 v110, v110, v111
	v_cvt_pk_f16_f32 v111, v112, v113
	v_cvt_pk_f16_f32 v112, v106, v107
	v_cvt_pk_f16_f32 v113, v108, v109
	v_mov_b32_e32 v218, v110
	v_mov_b32_e32 v219, v111
	v_mov_b32_e32 v220, v112
	v_mov_b32_e32 v221, v113
	s_nop 1
; __device__ __forceinline__ unsigned cvt_pk_f16(float lo, float hi) { f32x2 v = {lo, hi}; h16x2 b = __builtin_convertvector(v, h16x2); return __builtin_bit_cast(unsigned, b); }
;     __device__ __forceinline__ void operator()(const f32x4 (&acc)[2][2][4][2], const Unit& u, int wr, int wc, int fr, int fq) const {
;         const int row0 = u.pm * BM + wr * 64 + fr, col0 = u.pn * BM + wc * 32 + 8 * fq;
; #pragma unroll
;         for (int ai = 0; ai < 2; ++ai)
; #pragma unroll
;             for (int m = 0; m < 4; ++m) { h16* rowp = C + (size_t)(row0 + ai * HALF + m * 16) * ldc + col0;
; #pragma unroll
;                 for (int bj = 0; bj < 2; ++bj) { const f32x4 v0 = acc[ai][bj][m][0], v1 = acc[ai][bj][m][1];
;                     u32x4 w; w.x = cvt_pk_f16(v0[0], v0[1]); w.y = cvt_pk_f16(v0[2], v0[3]); w.z = cvt_pk_f16(v1[0], v1[1]); w.w = cvt_pk_f16(v1[2], v1[3]);
;                     *(u32x4*)(rowp + bj * HALF) = w; } }
	v_mov_b32_dpp v110, v126 row_ror:8 row_mask:0xf bank_mask:0x3
	v_mov_b32_dpp v111, v127 row_ror:8 row_mask:0xf bank_mask:0x3
	v_mov_b32_dpp v112, v128 row_ror:8 row_mask:0xf bank_mask:0x3
	v_mov_b32_dpp v113, v129 row_ror:8 row_mask:0xf bank_mask:0x3
	v_mov_b32_dpp v126, v218 row_ror:8 row_mask:0xf bank_mask:0xc
	v_mov_b32_dpp v127, v219 row_ror:8 row_mask:0xf bank_mask:0xc
	v_mov_b32_dpp v128, v220 row_ror:8 row_mask:0xf bank_mask:0xc
	v_mov_b32_dpp v129, v221 row_ror:8 row_mask:0xf bank_mask:0xc
	v_lshl_add_u64 v[168:169], v[152:153], 0, s[52:53]
	global_store_dwordx4 v[152:153], v[126:129], off
	global_store_dwordx4 v[168:169], v[110:113], off
	v_cvt_pk_f16_f32 v118, v118, v119
	v_cvt_pk_f16_f32 v119, v120, v121
	v_cvt_pk_f16_f32 v120, v114, v115
	v_cvt_pk_f16_f32 v121, v116, v117
	v_cvt_pk_f16_f32 v92, v92, v93
	v_cvt_pk_f16_f32 v93, v94, v95
	v_cvt_pk_f16_f32 v94, v88, v89
	v_cvt_pk_f16_f32 v95, v90, v91
	v_mov_b32_e32 v218, v92
	v_mov_b32_e32 v219, v93
	v_mov_b32_e32 v220, v94
	v_mov_b32_e32 v221, v95
	s_nop 1
	v_mov_b32_dpp v92, v118 row_ror:8 row_mask:0xf bank_mask:0x3
	v_mov_b32_dpp v93, v119 row_ror:8 row_mask:0xf bank_mask:0x3
	v_mov_b32_dpp v94, v120 row_ror:8 row_mask:0xf bank_mask:0x3
	v_mov_b32_dpp v95, v121 row_ror:8 row_mask:0xf bank_mask:0x3
	v_mov_b32_dpp v118, v218 row_ror:8 row_mask:0xf bank_mask:0xc
	v_mov_b32_dpp v119, v219 row_ror:8 row_mask:0xf bank_mask:0xc
	v_mov_b32_dpp v120, v220 row_ror:8 row_mask:0xf bank_mask:0xc
	v_mov_b32_dpp v121, v221 row_ror:8 row_mask:0xf bank_mask:0xc
	v_lshl_add_u64 v[168:169], v[154:155], 0, s[52:53]
	global_store_dwordx4 v[154:155], v[118:121], off
	global_store_dwordx4 v[168:169], v[92:95], off
	v_cvt_pk_f16_f32 v102, v102, v103
	v_cvt_pk_f16_f32 v103, v104, v105
	v_cvt_pk_f16_f32 v104, v98, v99
	v_cvt_pk_f16_f32 v105, v100, v101
	v_cvt_pk_f16_f32 v76, v76, v77
	v_cvt_pk_f16_f32 v77, v78, v79
	v_cvt_pk_f16_f32 v78, v72, v73
	v_cvt_pk_f16_f32 v79, v74, v75
	v_mov_b32_e32 v218, v76
	v_mov_b32_e32 v219, v77
	v_mov_b32_e32 v220, v78
	v_mov_b32_e32 v221, v79
	s_nop 1
	v_mov_b32_dpp v76, v102 row_ror:8 row_mask:0xf bank_mask:0x3
	v_mov_b32_dpp v77, v103 row_ror:8 row_mask:0xf bank_mask:0x3
	v_mov_b32_dpp v78, v104 row_ror:8 row_mask:0xf bank_mask:0x3
	v_mov_b32_dpp v79, v105 row_ror:8 row_mask:0xf bank_mask:0x3
	v_mov_b32_dpp v102, v218 row_ror:8 row_mask:0xf bank_mask:0xc
	v_mov_b32_dpp v103, v219 row_ror:8 row_mask:0xf bank_mask:0xc
	v_mov_b32_dpp v104, v220 row_ror:8 row_mask:0xf bank_mask:0xc
	v_mov_b32_dpp v105, v221 row_ror:8 row_mask:0xf bank_mask:0xc
	v_lshl_add_u64 v[168:169], v[156:157], 0, s[52:53]
	global_store_dwordx4 v[156:157], v[102:105], off
	global_store_dwordx4 v[168:169], v[76:79], off
	v_cvt_pk_f16_f32 v84, v84, v85
	v_cvt_pk_f16_f32 v85, v86, v87
	v_cvt_pk_f16_f32 v86, v80, v81
	v_cvt_pk_f16_f32 v87, v82, v83
	v_cvt_pk_f16_f32 v68, v68, v69
	v_cvt_pk_f16_f32 v69, v70, v71
	v_cvt_pk_f16_f32 v70, v64, v65
	v_cvt_pk_f16_f32 v71, v66, v67
	v_mov_b32_e32 v218, v68
	v_mov_b32_e32 v219, v69
	v_mov_b32_e32 v220, v70
	v_mov_b32_e32 v221, v71
	s_nop 1
	v_mov_b32_dpp v68, v84 row_ror:8 row_mask:0xf bank_mask:0x3
	v_mov_b32_dpp v69, v85 row_ror:8 row_mask:0xf bank_mask:0x3
	v_mov_b32_dpp v70, v86 row_ror:8 row_mask:0xf bank_mask:0x3
	v_mov_b32_dpp v71, v87 row_ror:8 row_mask:0xf bank_mask:0x3
	v_mov_b32_dpp v84, v218 row_ror:8 row_mask:0xf bank_mask:0xc
	v_mov_b32_dpp v85, v219 row_ror:8 row_mask:0xf bank_mask:0xc
	v_mov_b32_dpp v86, v220 row_ror:8 row_mask:0xf bank_mask:0xc
	v_mov_b32_dpp v87, v221 row_ror:8 row_mask:0xf bank_mask:0xc
	v_lshl_add_u64 v[168:169], v[158:159], 0, s[52:53]
	global_store_dwordx4 v[158:159], v[84:87], off
	global_store_dwordx4 v[168:169], v[68:71], off
	v_cvt_pk_f16_f32 v60, v60, v61
	v_cvt_pk_f16_f32 v61, v62, v63
	v_cvt_pk_f16_f32 v62, v56, v57
	v_cvt_pk_f16_f32 v63, v58, v59
	v_cvt_pk_f16_f32 v44, v44, v45
	v_cvt_pk_f16_f32 v45, v46, v47
	v_cvt_pk_f16_f32 v46, v40, v41
; __device__ __forceinline__ unsigned cvt_pk_f16(float lo, float hi) { f32x2 v = {lo, hi}; h16x2 b = __builtin_convertvector(v, h16x2); return __builtin_bit_cast(unsigned, b); }
;     __device__ __forceinline__ void operator()(const f32x4 (&acc)[2][2][4][2], const Unit& u, int wr, int wc, int fr, int fq) const {
;         const int row0 = u.pm * BM + wr * 64 + fr, col0 = u.pn * BM + wc * 32 + 8 * fq;
; #pragma unroll
;         for (int ai = 0; ai < 2; ++ai)
; #pragma unroll
;             for (int m = 0; m < 4; ++m) { h16* rowp = C + (size_t)(row0 + ai * HALF + m * 16) * ldc + col0;
; #pragma unroll
;                 for (int bj = 0; bj < 2; ++bj) { const f32x4 v0 = acc[ai][bj][m][0], v1 = acc[ai][bj][m][1];
;                     u32x4 w; w.x = cvt_pk_f16(v0[0], v0[1]); w.y = cvt_pk_f16(v0[2], v0[3]); w.z = cvt_pk_f16(v1[0], v1[1]); w.w = cvt_pk_f16(v1[2], v1[3]);
;                     *(u32x4*)(rowp + bj * HALF) = w; } }
	v_cvt_pk_f16_f32 v47, v42, v43
	v_mov_b32_e32 v218, v44
	v_mov_b32_e32 v219, v45
	v_mov_b32_e32 v220, v46
	v_mov_b32_e32 v221, v47
	s_nop 1
	v_mov_b32_dpp v44, v60 row_ror:8 row_mask:0xf bank_mask:0x3
	v_mov_b32_dpp v45, v61 row_ror:8 row_mask:0xf bank_mask:0x3
	v_mov_b32_dpp v46, v62 row_ror:8 row_mask:0xf bank_mask:0x3
	v_mov_b32_dpp v47, v63 row_ror:8 row_mask:0xf bank_mask:0x3
	v_mov_b32_dpp v60, v218 row_ror:8 row_mask:0xf bank_mask:0xc
	v_mov_b32_dpp v61, v219 row_ror:8 row_mask:0xf bank_mask:0xc
	v_mov_b32_dpp v62, v220 row_ror:8 row_mask:0xf bank_mask:0xc
	v_mov_b32_dpp v63, v221 row_ror:8 row_mask:0xf bank_mask:0xc
	v_lshl_add_u64 v[168:169], v[160:161], 0, s[52:53]
	global_store_dwordx4 v[160:161], v[60:63], off
	global_store_dwordx4 v[168:169], v[44:47], off
	v_cvt_pk_f16_f32 v52, v52, v53
	v_cvt_pk_f16_f32 v53, v54, v55
	v_cvt_pk_f16_f32 v54, v48, v49
	v_cvt_pk_f16_f32 v55, v50, v51
	v_cvt_pk_f16_f32 v28, v28, v29
	v_cvt_pk_f16_f32 v29, v30, v31
	v_cvt_pk_f16_f32 v30, v24, v25
	v_cvt_pk_f16_f32 v31, v26, v27
	v_mov_b32_e32 v218, v28
	v_mov_b32_e32 v219, v29
	v_mov_b32_e32 v220, v30
	v_mov_b32_e32 v221, v31
	s_nop 1
	v_mov_b32_dpp v28, v52 row_ror:8 row_mask:0xf bank_mask:0x3
	v_mov_b32_dpp v29, v53 row_ror:8 row_mask:0xf bank_mask:0x3
	v_mov_b32_dpp v30, v54 row_ror:8 row_mask:0xf bank_mask:0x3
	v_mov_b32_dpp v31, v55 row_ror:8 row_mask:0xf bank_mask:0x3
	v_mov_b32_dpp v52, v218 row_ror:8 row_mask:0xf bank_mask:0xc
	v_mov_b32_dpp v53, v219 row_ror:8 row_mask:0xf bank_mask:0xc
	v_mov_b32_dpp v54, v220 row_ror:8 row_mask:0xf bank_mask:0xc
	v_mov_b32_dpp v55, v221 row_ror:8 row_mask:0xf bank_mask:0xc
	v_lshl_add_u64 v[168:169], v[162:163], 0, s[52:53]
	global_store_dwordx4 v[162:163], v[52:55], off
	global_store_dwordx4 v[168:169], v[28:31], off
	v_cvt_pk_f16_f32 v36, v36, v37
	v_cvt_pk_f16_f32 v37, v38, v39
	v_cvt_pk_f16_f32 v38, v32, v33
	v_cvt_pk_f16_f32 v39, v34, v35
	v_cvt_pk_f16_f32 v12, v12, v13
	v_cvt_pk_f16_f32 v13, v14, v15
	v_cvt_pk_f16_f32 v14, v8, v9
	v_cvt_pk_f16_f32 v15, v10, v11
	v_mov_b32_e32 v218, v12
	v_mov_b32_e32 v219, v13
	v_mov_b32_e32 v220, v14
	v_mov_b32_e32 v221, v15
	s_nop 1
	v_mov_b32_dpp v12, v36 row_ror:8 row_mask:0xf bank_mask:0x3
	v_mov_b32_dpp v13, v37 row_ror:8 row_mask:0xf bank_mask:0x3
	v_mov_b32_dpp v14, v38 row_ror:8 row_mask:0xf bank_mask:0x3
	v_mov_b32_dpp v15, v39 row_ror:8 row_mask:0xf bank_mask:0x3
	v_mov_b32_dpp v36, v218 row_ror:8 row_mask:0xf bank_mask:0xc
	v_mov_b32_dpp v37, v219 row_ror:8 row_mask:0xf bank_mask:0xc
	v_mov_b32_dpp v38, v220 row_ror:8 row_mask:0xf bank_mask:0xc
	v_mov_b32_dpp v39, v221 row_ror:8 row_mask:0xf bank_mask:0xc
	v_lshl_add_u64 v[168:169], v[164:165], 0, s[52:53]
	global_store_dwordx4 v[164:165], v[36:39], off
	global_store_dwordx4 v[168:169], v[12:15], off
	v_cvt_pk_f16_f32 v20, v20, v21
	v_cvt_pk_f16_f32 v21, v22, v23
	v_cvt_pk_f16_f32 v22, v16, v17
	v_cvt_pk_f16_f32 v23, v18, v19
	v_cvt_pk_f16_f32 v4, v4, v5
	v_cvt_pk_f16_f32 v5, v6, v7
	v_cvt_pk_f16_f32 v6, v0, v1
	v_cvt_pk_f16_f32 v7, v2, v3
	v_mov_b32_e32 v218, v4
	v_mov_b32_e32 v219, v5
	v_mov_b32_e32 v220, v6
	v_mov_b32_e32 v221, v7
	s_nop 1
	v_mov_b32_dpp v4, v20 row_ror:8 row_mask:0xf bank_mask:0x3
	v_mov_b32_dpp v5, v21 row_ror:8 row_mask:0xf bank_mask:0x3
	v_mov_b32_dpp v6, v22 row_ror:8 row_mask:0xf bank_mask:0x3
	v_mov_b32_dpp v7, v23 row_ror:8 row_mask:0xf bank_mask:0x3
	v_mov_b32_dpp v20, v218 row_ror:8 row_mask:0xf bank_mask:0xc
	v_mov_b32_dpp v21, v219 row_ror:8 row_mask:0xf bank_mask:0xc
	v_mov_b32_dpp v22, v220 row_ror:8 row_mask:0xf bank_mask:0xc
	v_mov_b32_dpp v23, v221 row_ror:8 row_mask:0xf bank_mask:0xc
	v_lshl_add_u64 v[168:169], v[166:167], 0, s[52:53]
	global_store_dwordx4 v[166:167], v[20:23], off
	global_store_dwordx4 v[168:169], v[4:7], off
	s_andn2_b64 vcc, exec, s[38:39]
	s_mov_b64 s[38:39], -1
	s_mov_b32 s44, 0x800000
	s_cbranch_vccnz .LBB0_976
	s_andn2_b64 vcc, exec, s[0:1]
	s_cbranch_vccnz .LBB0_975
	s_barrier
	s_branch .LBB0_975
